# baseline (speedup 1.0000x reference)
.LBB0_20:
	s_or_b64 exec, exec, s[8:9]
	v_add_f32_e32 v2, v44, v4
	s_nop 1
	v_max_f32_dpp v2, v2, v2 quad_perm:[1,0,3,2] row_mask:0xf bank_mask:0xf
	s_nop 1
	v_max_f32_dpp v2, v2, v2 quad_perm:[2,3,0,1] row_mask:0xf bank_mask:0xf
	s_nop 1
	v_max_f32_dpp v2, v2, v2 row_half_mirror row_mask:0xf bank_mask:0xf
	s_nop 1
	v_max_f32_dpp v2, v2, v2 row_mirror row_mask:0xf bank_mask:0xf
	s_nop 1
	v_max_f32_dpp v2, v2, v2 row_bcast:15 row_mask:0xa bank_mask:0xf
	s_nop 1
	v_max_f32_dpp v2, v2, v2 row_bcast:31 row_mask:0xc bank_mask:0xf
	s_nop 1
	v_readlane_b32 s20, v2, 63
	s_nop 3
	v_mov_b32_e32 v2, s20
	v_mov_b32_e32 v3, s20
	v_cmp_eq_u32_e32 vcc, 0, v1
	s_and_saveexec_b64 s[2:3], vcc
	s_cbranch_execz .LBB0_22
	s_mov_b64 s[8:9], s[30:31]
	s_waitcnt lgkmcnt(0)
	v_max_f32_e32 v3, v3, v3
	v_max_f32_e32 v2, v2, v2
	v_mov_b32_e32 v19, 0
	v_max_f32_e32 v4, v2, v3
	v_lshl_add_u64 v[2:3], v[18:19], 2, s[8:9]
	global_store_dword v[2:3], v4, off sc1
